# v16 + S5 carry-scan recurrence rewritten: two dependent packed FMAs per step, LDS reads 4 steps ahead, one v_cvt_pk_bf16 per state pair
# speedup vs baseline: 1.0035x; 1.0017x over previous
.LBB0_603:
	s_mov_b64 s[76:77], 0x10000
	s_or_b64 exec, exec, s[24:25]
	v_cmp_gt_i32_e32 vcc, 64, v6
	s_waitcnt lgkmcnt(0)
	s_barrier
	s_and_saveexec_b64 s[40:41], vcc
	s_cbranch_execz .LBB0_607
	v_readlane_b32 s0, v253, 32
	v_readlane_b32 s1, v253, 33
	s_lshl_b64 s[2:3], s[0:1], 13
	s_add_u32 s2, s14, s2
	s_addc_u32 s3, s15, s3
	s_lshl_b32 s12, s38, 7
	v_lshl_add_u32 v2, v6, 1, s12
	v_ashrrev_i32_e32 v3, 31, v2
	v_lshl_add_u64 v[2:3], v[2:3], 2, s[2:3]
	v_add_co_u32_e32 v2, vcc, 0x4e00000, v2
	s_and_b32 s12, s88, 7
	s_nop 0
	v_addc_co_u32_e32 v3, vcc, 0, v3, vcc
	global_load_dwordx2 v[2:3], v[2:3], off
	s_add_i32 s2, 0, 0x1000
	s_mul_i32 s3, s38, 0x180000
	s_mul_i32 s12, s12, 0x30000
	v_lshl_add_u32 v1, v6, 2, s2
	s_mul_hi_i32 s2, s38, 0x180000
	s_add_u32 s3, s3, s12
	s_addc_u32 s12, s2, 0
	s_add_u32 s2, s42, s3
	s_addc_u32 s3, s43, s12
	v_lshl_add_u64 v[6:7], v[6:7], 1, s[2:3]
	v_mov_b32_e32 v8, 0
	s_mov_b64 s[42:43], 0
	v_mov_b32_e32 v12, 0
	s_waitcnt vmcnt(0) lgkmcnt(0)
	v_pk_mov_b32 v[4:5], v[2:3], v[2:3] op_sel:[1,0]
	v_mov_b32_e32 v9, 0
	ds_read2st64_b32 v[20:21], v1 offset1:1
	ds_read2st64_b32 v[22:23], v1 offset0:2 offset1:3
	ds_read2st64_b32 v[24:25], v1 offset0:4 offset1:5
	ds_read2st64_b32 v[26:27], v1 offset0:6 offset1:7
.LBB0_605:
	v_lshl_add_u64 v[10:11], v[6:7], 0, s[42:43]
	v_add_co_u32_e32 v16, vcc, 0x61000000, v10
	s_mov_b32 s2, 0x61001000
	s_nop 1
	v_addc_co_u32_e32 v17, vcc, 0, v11, vcc
	v_add_co_u32_e32 v10, vcc, s2, v10
	s_nop 1
	v_addc_co_u32_e32 v11, vcc, 0, v11, vcc
	v_cvt_pk_bf16_f32 v30, v8, v9
	s_waitcnt lgkmcnt(3)
	v_pk_fma_f32 v[28:29], v[2:3], v[8:9], v[20:21] op_sel_hi:[0,1,1]
	global_store_short v[16:17], v30, off offset:512
	global_store_short_d16_hi v[16:17], v30, off offset:640
	v_pk_fma_f32 v[8:9], v[2:3], v[8:9], v[28:29] op_sel:[1,1,0] op_sel_hi:[1,0,1] neg_lo:[1,0,0]
	ds_read2st64_b32 v[20:21], v1 offset0:8 offset1:9
	v_cvt_pk_bf16_f32 v31, v8, v9
	s_waitcnt lgkmcnt(3)
	v_pk_fma_f32 v[28:29], v[2:3], v[8:9], v[22:23] op_sel_hi:[0,1,1]
	global_store_short v[16:17], v31, off offset:1280
	global_store_short_d16_hi v[16:17], v31, off offset:1408
	v_pk_fma_f32 v[8:9], v[2:3], v[8:9], v[28:29] op_sel:[1,1,0] op_sel_hi:[1,0,1] neg_lo:[1,0,0]
	ds_read2st64_b32 v[22:23], v1 offset0:10 offset1:11
	v_cvt_pk_bf16_f32 v30, v8, v9
	s_waitcnt lgkmcnt(3)
	v_pk_fma_f32 v[28:29], v[2:3], v[8:9], v[24:25] op_sel_hi:[0,1,1]
	global_store_short v[16:17], v30, off offset:2048
	global_store_short_d16_hi v[16:17], v30, off offset:2176
	v_pk_fma_f32 v[8:9], v[2:3], v[8:9], v[28:29] op_sel:[1,1,0] op_sel_hi:[1,0,1] neg_lo:[1,0,0]
	ds_read2st64_b32 v[24:25], v1 offset0:12 offset1:13
	v_cvt_pk_bf16_f32 v31, v8, v9
	s_waitcnt lgkmcnt(3)
	v_pk_fma_f32 v[28:29], v[2:3], v[8:9], v[26:27] op_sel_hi:[0,1,1]
	global_store_short v[16:17], v31, off offset:2816
	global_store_short_d16_hi v[16:17], v31, off offset:2944
	v_pk_fma_f32 v[8:9], v[2:3], v[8:9], v[28:29] op_sel:[1,1,0] op_sel_hi:[1,0,1] neg_lo:[1,0,0]
	ds_read2st64_b32 v[26:27], v1 offset0:14 offset1:15
	v_cvt_pk_bf16_f32 v30, v8, v9
	s_waitcnt lgkmcnt(3)
	v_pk_fma_f32 v[28:29], v[2:3], v[8:9], v[20:21] op_sel_hi:[0,1,1]
	global_store_short v[16:17], v30, off offset:3584
	global_store_short_d16_hi v[16:17], v30, off offset:3712
	v_pk_fma_f32 v[8:9], v[2:3], v[8:9], v[28:29] op_sel:[1,1,0] op_sel_hi:[1,0,1] neg_lo:[1,0,0]
	ds_read2st64_b32 v[20:21], v1 offset0:16 offset1:17
	v_cvt_pk_bf16_f32 v31, v8, v9
	s_waitcnt lgkmcnt(3)
	v_pk_fma_f32 v[28:29], v[2:3], v[8:9], v[22:23] op_sel_hi:[0,1,1]
	global_store_short v[10:11], v31, off offset:256
	global_store_short_d16_hi v[10:11], v31, off offset:384
	v_pk_fma_f32 v[8:9], v[2:3], v[8:9], v[28:29] op_sel:[1,1,0] op_sel_hi:[1,0,1] neg_lo:[1,0,0]
	ds_read2st64_b32 v[22:23], v1 offset0:18 offset1:19
	v_cvt_pk_bf16_f32 v30, v8, v9
	s_waitcnt lgkmcnt(3)
	v_pk_fma_f32 v[28:29], v[2:3], v[8:9], v[24:25] op_sel_hi:[0,1,1]
	global_store_short v[10:11], v30, off offset:1024
	global_store_short_d16_hi v[10:11], v30, off offset:1152
	v_pk_fma_f32 v[8:9], v[2:3], v[8:9], v[28:29] op_sel:[1,1,0] op_sel_hi:[1,0,1] neg_lo:[1,0,0]
	ds_read2st64_b32 v[24:25], v1 offset0:20 offset1:21
	v_cvt_pk_bf16_f32 v31, v8, v9
	s_waitcnt lgkmcnt(3)
	v_pk_fma_f32 v[28:29], v[2:3], v[8:9], v[26:27] op_sel_hi:[0,1,1]
	global_store_short v[10:11], v31, off offset:1792
	global_store_short_d16_hi v[10:11], v31, off offset:1920
	v_pk_fma_f32 v[8:9], v[2:3], v[8:9], v[28:29] op_sel:[1,1,0] op_sel_hi:[1,0,1] neg_lo:[1,0,0]
	ds_read2st64_b32 v[26:27], v1 offset0:22 offset1:23
	v_add_u32_e32 v1, 0x1000, v1
	s_add_u32 s42, s42, 0x1800
	s_addc_u32 s43, s43, 0
	s_cmp_eq_u32 s42, 0x30000
	s_cbranch_scc0 .LBB0_605
	s_waitcnt lgkmcnt(0)
	s_waitcnt vmcnt(0)
	s_waitcnt vmcnt(0)
	buffer_inv sc1
	s_waitcnt vmcnt(0)
